# RG-LRU: backward direction's weight fragments requested right after the forward direction's last MFMAs
# baseline (speedup 1.0000x reference)
.Lmylru_nodma_4:
	v_or_b32_e32 v163, 0x10000, v162
	ds_read_b128 v[96:99], v163
	ds_read_b128 v[100:103], v163 offset:8192
	ds_read_b128 v[104:107], v163 offset:16384
	ds_read_b128 v[108:111], v163 offset:24576
	v_xor_b32_e32 v164, 0x40, v163
	ds_read_b128 v[112:115], v164
	ds_read_b128 v[116:119], v164 offset:8192
	ds_read_b128 v[120:123], v164 offset:16384
	ds_read_b128 v[124:127], v164 offset:24576
	s_waitcnt lgkmcnt(7)
	v_mfma_f32_16x16x32_bf16 v[64:67], v[96:99], v[0:3], 0
	v_mfma_f32_16x16x32_bf16 v[68:71], v[96:99], v[32:35], 0
	v_xor_b32_e32 v164, 0x80, v163
	ds_read_b128 v[96:99], v164
	s_waitcnt lgkmcnt(7)
	v_mfma_f32_16x16x32_bf16 v[72:75], v[100:103], v[0:3], 0
	v_mfma_f32_16x16x32_bf16 v[76:79], v[100:103], v[32:35], 0
	ds_read_b128 v[100:103], v164 offset:8192
	s_waitcnt lgkmcnt(7)
	v_mfma_f32_16x16x32_bf16 v[80:83], v[104:107], v[0:3], 0
	v_mfma_f32_16x16x32_bf16 v[84:87], v[104:107], v[32:35], 0
	ds_read_b128 v[104:107], v164 offset:16384
	s_waitcnt lgkmcnt(7)
	v_mfma_f32_16x16x32_bf16 v[88:91], v[108:111], v[0:3], 0
	v_mfma_f32_16x16x32_bf16 v[92:95], v[108:111], v[32:35], 0
	ds_read_b128 v[108:111], v164 offset:24576
	s_waitcnt lgkmcnt(7)
	v_mfma_f32_16x16x32_bf16 v[64:67], v[112:115], v[4:7], v[64:67]
	v_mfma_f32_16x16x32_bf16 v[68:71], v[112:115], v[36:39], v[68:71]
	v_xor_b32_e32 v164, 0xc0, v163
	ds_read_b128 v[112:115], v164
	s_waitcnt lgkmcnt(7)
	v_mfma_f32_16x16x32_bf16 v[72:75], v[116:119], v[4:7], v[72:75]
	v_mfma_f32_16x16x32_bf16 v[76:79], v[116:119], v[36:39], v[76:79]
	ds_read_b128 v[116:119], v164 offset:8192
	s_waitcnt lgkmcnt(7)
	v_mfma_f32_16x16x32_bf16 v[80:83], v[120:123], v[4:7], v[80:83]
	v_mfma_f32_16x16x32_bf16 v[84:87], v[120:123], v[36:39], v[84:87]
	ds_read_b128 v[120:123], v164 offset:16384
	s_waitcnt lgkmcnt(7)
	v_mfma_f32_16x16x32_bf16 v[88:91], v[124:127], v[4:7], v[88:91]
	v_mfma_f32_16x16x32_bf16 v[92:95], v[124:127], v[36:39], v[92:95]
	ds_read_b128 v[124:127], v164 offset:24576
	s_waitcnt lgkmcnt(7)
	v_mfma_f32_16x16x32_bf16 v[64:67], v[96:99], v[8:11], v[64:67]
	v_mfma_f32_16x16x32_bf16 v[68:71], v[96:99], v[40:43], v[68:71]
	v_xor_b32_e32 v164, 0x100, v163
	ds_read_b128 v[96:99], v164
	s_waitcnt lgkmcnt(7)
	v_mfma_f32_16x16x32_bf16 v[72:75], v[100:103], v[8:11], v[72:75]
	v_mfma_f32_16x16x32_bf16 v[76:79], v[100:103], v[40:43], v[76:79]
	ds_read_b128 v[100:103], v164 offset:8192
	s_waitcnt lgkmcnt(7)
	v_mfma_f32_16x16x32_bf16 v[80:83], v[104:107], v[8:11], v[80:83]
	v_mfma_f32_16x16x32_bf16 v[84:87], v[104:107], v[40:43], v[84:87]
	ds_read_b128 v[104:107], v164 offset:16384
	s_waitcnt lgkmcnt(7)
	v_mfma_f32_16x16x32_bf16 v[88:91], v[108:111], v[8:11], v[88:91]
	v_mfma_f32_16x16x32_bf16 v[92:95], v[108:111], v[40:43], v[92:95]
	ds_read_b128 v[108:111], v164 offset:24576
	s_waitcnt lgkmcnt(7)
	v_mfma_f32_16x16x32_bf16 v[64:67], v[112:115], v[12:15], v[64:67]
	v_mfma_f32_16x16x32_bf16 v[68:71], v[112:115], v[44:47], v[68:71]
	v_xor_b32_e32 v164, 0x140, v163
	ds_read_b128 v[112:115], v164
	s_waitcnt lgkmcnt(7)
	v_mfma_f32_16x16x32_bf16 v[72:75], v[116:119], v[12:15], v[72:75]
	v_mfma_f32_16x16x32_bf16 v[76:79], v[116:119], v[44:47], v[76:79]
	ds_read_b128 v[116:119], v164 offset:8192
	s_waitcnt lgkmcnt(7)
	v_mfma_f32_16x16x32_bf16 v[80:83], v[120:123], v[12:15], v[80:83]
	v_mfma_f32_16x16x32_bf16 v[84:87], v[120:123], v[44:47], v[84:87]
	ds_read_b128 v[120:123], v164 offset:16384
	s_waitcnt lgkmcnt(7)
	v_mfma_f32_16x16x32_bf16 v[88:91], v[124:127], v[12:15], v[88:91]
	v_mfma_f32_16x16x32_bf16 v[92:95], v[124:127], v[44:47], v[92:95]
	ds_read_b128 v[124:127], v164 offset:24576
	s_waitcnt lgkmcnt(7)
	v_mfma_f32_16x16x32_bf16 v[64:67], v[96:99], v[16:19], v[64:67]
	v_mfma_f32_16x16x32_bf16 v[68:71], v[96:99], v[48:51], v[68:71]
	v_xor_b32_e32 v164, 0x180, v163
	ds_read_b128 v[96:99], v164
	s_waitcnt lgkmcnt(7)
	v_mfma_f32_16x16x32_bf16 v[72:75], v[100:103], v[16:19], v[72:75]
	v_mfma_f32_16x16x32_bf16 v[76:79], v[100:103], v[48:51], v[76:79]
	ds_read_b128 v[100:103], v164 offset:8192
	s_waitcnt lgkmcnt(7)
	v_mfma_f32_16x16x32_bf16 v[80:83], v[104:107], v[16:19], v[80:83]
	v_mfma_f32_16x16x32_bf16 v[84:87], v[104:107], v[48:51], v[84:87]
	ds_read_b128 v[104:107], v164 offset:16384
	s_waitcnt lgkmcnt(7)
	v_mfma_f32_16x16x32_bf16 v[88:91], v[108:111], v[16:19], v[88:91]
	v_mfma_f32_16x16x32_bf16 v[92:95], v[108:111], v[48:51], v[92:95]
	ds_read_b128 v[108:111], v164 offset:24576
	s_waitcnt lgkmcnt(7)
	v_mfma_f32_16x16x32_bf16 v[64:67], v[112:115], v[20:23], v[64:67]
	v_mfma_f32_16x16x32_bf16 v[68:71], v[112:115], v[52:55], v[68:71]
	v_xor_b32_e32 v164, 0x1c0, v163
	ds_read_b128 v[112:115], v164
	s_waitcnt lgkmcnt(7)
	v_mfma_f32_16x16x32_bf16 v[72:75], v[116:119], v[20:23], v[72:75]
	v_mfma_f32_16x16x32_bf16 v[76:79], v[116:119], v[52:55], v[76:79]
	ds_read_b128 v[116:119], v164 offset:8192
	s_waitcnt lgkmcnt(7)
	v_mfma_f32_16x16x32_bf16 v[80:83], v[120:123], v[20:23], v[80:83]
	v_mfma_f32_16x16x32_bf16 v[84:87], v[120:123], v[52:55], v[84:87]
	ds_read_b128 v[120:123], v164 offset:16384
	s_waitcnt lgkmcnt(7)
	v_mfma_f32_16x16x32_bf16 v[88:91], v[124:127], v[20:23], v[88:91]
	v_mfma_f32_16x16x32_bf16 v[92:95], v[124:127], v[52:55], v[92:95]
	ds_read_b128 v[124:127], v164 offset:24576
	s_waitcnt lgkmcnt(7)
	v_mfma_f32_16x16x32_bf16 v[64:67], v[96:99], v[24:27], v[64:67]
	v_mfma_f32_16x16x32_bf16 v[68:71], v[96:99], v[56:59], v[68:71]
	s_waitcnt lgkmcnt(6)
	v_mfma_f32_16x16x32_bf16 v[72:75], v[100:103], v[24:27], v[72:75]
	v_mfma_f32_16x16x32_bf16 v[76:79], v[100:103], v[56:59], v[76:79]
	s_waitcnt lgkmcnt(5)
	v_mfma_f32_16x16x32_bf16 v[80:83], v[104:107], v[24:27], v[80:83]
	v_mfma_f32_16x16x32_bf16 v[84:87], v[104:107], v[56:59], v[84:87]
	s_waitcnt lgkmcnt(4)
	v_mfma_f32_16x16x32_bf16 v[88:91], v[108:111], v[24:27], v[88:91]
	v_mfma_f32_16x16x32_bf16 v[92:95], v[108:111], v[56:59], v[92:95]
	s_waitcnt lgkmcnt(3)
	v_mfma_f32_16x16x32_bf16 v[64:67], v[112:115], v[28:31], v[64:67]
	v_mfma_f32_16x16x32_bf16 v[68:71], v[112:115], v[60:63], v[68:71]
	s_waitcnt lgkmcnt(2)
	v_mfma_f32_16x16x32_bf16 v[72:75], v[116:119], v[28:31], v[72:75]
	v_mfma_f32_16x16x32_bf16 v[76:79], v[116:119], v[60:63], v[76:79]
	s_waitcnt lgkmcnt(1)
	v_mfma_f32_16x16x32_bf16 v[80:83], v[120:123], v[28:31], v[80:83]
	v_mfma_f32_16x16x32_bf16 v[84:87], v[120:123], v[60:63], v[84:87]
	s_waitcnt lgkmcnt(0)
	v_mfma_f32_16x16x32_bf16 v[88:91], v[124:127], v[28:31], v[88:91]
	v_mfma_f32_16x16x32_bf16 v[92:95], v[124:127], v[60:63], v[92:95]
	s_cmp_eq_u32 s13, 17
	s_cbranch_scc0 .Lmylru_nw_4
	s_lshl_b32 s50, s10, 10
	s_lshl_b32 s51, s11, 6
	s_add_i32 s50, s50, s51
	s_lshl_b32 s51, s8, 4
	s_add_i32 s50, s50, s51
	s_add_i32 s50, s50, 512
	s_lshl_b32 s50, s50, 9
	s_add_u32 s46, s2, s50
	s_addc_u32 s47, s3, 0
	s_add_u32 s46, s46, 0x1000000
	s_addc_u32 s47, s47, 0
	s_add_u32 s48, s46, 0x20000
	s_addc_u32 s49, s47, 0
	v_lshlrev_b32_e32 v255, 9, v160
	v_lshl_add_u32 v255, v161, 4, v255
	global_load_dwordx4 v[0:3], v255, s[46:47]
	global_load_dwordx4 v[4:7], v255, s[46:47] offset:64
	global_load_dwordx4 v[8:11], v255, s[46:47] offset:128
	global_load_dwordx4 v[12:15], v255, s[46:47] offset:192
	global_load_dwordx4 v[16:19], v255, s[46:47] offset:256
	global_load_dwordx4 v[20:23], v255, s[46:47] offset:320
	global_load_dwordx4 v[24:27], v255, s[46:47] offset:384
	global_load_dwordx4 v[28:31], v255, s[46:47] offset:448
	global_load_dwordx4 v[32:35], v255, s[48:49]
	global_load_dwordx4 v[36:39], v255, s[48:49] offset:64
	global_load_dwordx4 v[40:43], v255, s[48:49] offset:128
	global_load_dwordx4 v[44:47], v255, s[48:49] offset:192
	global_load_dwordx4 v[48:51], v255, s[48:49] offset:256
	global_load_dwordx4 v[52:55], v255, s[48:49] offset:320
	global_load_dwordx4 v[56:59], v255, s[48:49] offset:384
	global_load_dwordx4 v[60:63], v255, s[48:49] offset:448
.Lmylru_nw_4:
	v_or_b32_e32 v169, 0x10000, v165
	v_or_b32_e32 v170, 0x10000, v166
	v_or_b32_e32 v171, 0x10000, v167
	v_or_b32_e32 v172, 0x10000, v168
	ds_read_u16 v144, v169
	ds_read_u16 v145, v170
	ds_read_u16 v146, v171
	ds_read_u16 v147, v172
	ds_read_u16 v148, v169 offset:8192
	ds_read_u16 v149, v170 offset:8192
	ds_read_u16 v150, v171 offset:8192
	ds_read_u16 v151, v172 offset:8192
	ds_read_u16 v152, v169 offset:16384
	ds_read_u16 v153, v170 offset:16384
	ds_read_u16 v154, v171 offset:16384
	ds_read_u16 v155, v172 offset:16384
	ds_read_u16 v156, v169 offset:24576
	ds_read_u16 v157, v170 offset:24576
	ds_read_u16 v158, v171 offset:24576
	ds_read_u16 v159, v172 offset:24576
	s_nop 7
	v_fma_f32 v178, v64, s53, v173
	v_fma_f32 v179, v65, s53, v173
	v_fma_f32 v180, v66, s53, v173
	v_fma_f32 v181, v67, s53, v173
	v_fma_f32 v182, v72, s53, v173
	v_fma_f32 v183, v73, s53, v173
	v_fma_f32 v184, v74, s53, v173
	v_fma_f32 v185, v75, s53, v173
	v_fma_f32 v186, v68, s53, v174
	v_fma_f32 v187, v69, s53, v174
	v_fma_f32 v188, v70, s53, v174
	v_fma_f32 v189, v71, s53, v174
	v_fma_f32 v190, v76, s53, v174
	v_fma_f32 v191, v77, s53, v174
	v_fma_f32 v192, v78, s53, v174
	v_fma_f32 v193, v79, s53, v174
	v_exp_f32_e32 v178, v178
	v_exp_f32_e32 v179, v179
	v_exp_f32_e32 v180, v180
	v_exp_f32_e32 v181, v181
	v_exp_f32_e32 v182, v182
	v_exp_f32_e32 v183, v183
	v_exp_f32_e32 v184, v184
	v_exp_f32_e32 v185, v185
	v_exp_f32_e32 v186, v186
	v_exp_f32_e32 v187, v187
	v_exp_f32_e32 v188, v188
	v_exp_f32_e32 v189, v189
	v_exp_f32_e32 v190, v190
	v_exp_f32_e32 v191, v191
	v_exp_f32_e32 v192, v192
	v_exp_f32_e32 v193, v193
	v_add_f32_e32 v178, 1.0, v178
	v_add_f32_e32 v179, 1.0, v179
	v_add_f32_e32 v180, 1.0, v180
	v_add_f32_e32 v181, 1.0, v181
	v_add_f32_e32 v182, 1.0, v182
	v_add_f32_e32 v183, 1.0, v183
	v_add_f32_e32 v184, 1.0, v184
	v_add_f32_e32 v185, 1.0, v185
	v_add_f32_e32 v186, 1.0, v186
	v_add_f32_e32 v187, 1.0, v187
	v_add_f32_e32 v188, 1.0, v188
	v_add_f32_e32 v189, 1.0, v189
	v_add_f32_e32 v190, 1.0, v190
	v_add_f32_e32 v191, 1.0, v191
	v_add_f32_e32 v192, 1.0, v192
	v_add_f32_e32 v193, 1.0, v193
	v_rcp_f32_e32 v178, v178
	v_rcp_f32_e32 v179, v179
	v_rcp_f32_e32 v180, v180
	v_rcp_f32_e32 v181, v181
	v_rcp_f32_e32 v182, v182
	v_rcp_f32_e32 v183, v183
	v_rcp_f32_e32 v184, v184
	v_rcp_f32_e32 v185, v185
	v_rcp_f32_e32 v186, v186
	v_rcp_f32_e32 v187, v187
	v_rcp_f32_e32 v188, v188
	v_rcp_f32_e32 v189, v189
	v_rcp_f32_e32 v190, v190
	v_rcp_f32_e32 v191, v191
	v_rcp_f32_e32 v192, v192
	v_rcp_f32_e32 v193, v193
	v_mul_f32_e32 v178, v175, v178
	v_mul_f32_e32 v179, v175, v179
	v_mul_f32_e32 v180, v175, v180
	v_mul_f32_e32 v181, v175, v181
	v_mul_f32_e32 v182, v175, v182
	v_mul_f32_e32 v183, v175, v183
	v_mul_f32_e32 v184, v175, v184
	v_mul_f32_e32 v185, v175, v185
	v_exp_f32_e32 v96, v178
	v_exp_f32_e32 v97, v179
	v_exp_f32_e32 v98, v180
	v_exp_f32_e32 v99, v181
	v_exp_f32_e32 v100, v182
	v_exp_f32_e32 v101, v183
	v_exp_f32_e32 v102, v184
	v_exp_f32_e32 v103, v185
	s_nop 0
	v_fma_f32 v194, -v96, v96, 1.0
	v_fma_f32 v195, -v97, v97, 1.0
	v_fma_f32 v196, -v98, v98, 1.0
	v_fma_f32 v197, -v99, v99, 1.0
	v_fma_f32 v198, -v100, v100, 1.0
	v_fma_f32 v199, -v101, v101, 1.0
	v_fma_f32 v200, -v102, v102, 1.0
	v_fma_f32 v201, -v103, v103, 1.0
	v_max_f32_e32 v194, 0, v194
	v_max_f32_e32 v195, 0, v195
	v_max_f32_e32 v196, 0, v196
	v_max_f32_e32 v197, 0, v197
	v_max_f32_e32 v198, 0, v198
	v_max_f32_e32 v199, 0, v199
	v_max_f32_e32 v200, 0, v200
	v_max_f32_e32 v201, 0, v201
	v_sqrt_f32_e32 v194, v194
	v_sqrt_f32_e32 v195, v195
	v_sqrt_f32_e32 v196, v196
	v_sqrt_f32_e32 v197, v197
	v_sqrt_f32_e32 v198, v198
	v_sqrt_f32_e32 v199, v199
	v_sqrt_f32_e32 v200, v200
	v_sqrt_f32_e32 v201, v201
	s_waitcnt lgkmcnt(8)
	v_lshlrev_b32_e32 v144, 16, v144
	v_lshlrev_b32_e32 v145, 16, v145
	v_lshlrev_b32_e32 v146, 16, v146
	v_lshlrev_b32_e32 v147, 16, v147
	v_lshlrev_b32_e32 v148, 16, v148
	v_lshlrev_b32_e32 v149, 16, v149
	v_lshlrev_b32_e32 v150, 16, v150
	v_lshlrev_b32_e32 v151, 16, v151
	v_mul_f32_e32 v194, v194, v186
	v_mul_f32_e32 v195, v195, v187
	v_mul_f32_e32 v196, v196, v188
	v_mul_f32_e32 v197, v197, v189
	v_mul_f32_e32 v198, v198, v190
	v_mul_f32_e32 v199, v199, v191
	v_mul_f32_e32 v200, v200, v192
	v_mul_f32_e32 v201, v201, v193
	v_mul_f32_e32 v144, v194, v144
	v_mul_f32_e32 v145, v195, v145
	v_mul_f32_e32 v146, v196, v146
	v_mul_f32_e32 v147, v197, v147
	v_mul_f32_e32 v148, v198, v148
	v_mul_f32_e32 v149, v199, v149
	v_mul_f32_e32 v150, v200, v150
	v_mul_f32_e32 v151, v201, v151
	v_fma_f32 v178, v80, s53, v173
	v_fma_f32 v179, v81, s53, v173
	v_fma_f32 v180, v82, s53, v173
	v_fma_f32 v181, v83, s53, v173
	v_fma_f32 v182, v88, s53, v173
	v_fma_f32 v183, v89, s53, v173
	v_fma_f32 v184, v90, s53, v173
	v_fma_f32 v185, v91, s53, v173
	v_fma_f32 v186, v84, s53, v174
	v_fma_f32 v187, v85, s53, v174
	v_fma_f32 v188, v86, s53, v174
	v_fma_f32 v189, v87, s53, v174
	v_fma_f32 v190, v92, s53, v174
	v_fma_f32 v191, v93, s53, v174
	v_fma_f32 v192, v94, s53, v174
	v_fma_f32 v193, v95, s53, v174
	v_exp_f32_e32 v178, v178
	v_exp_f32_e32 v179, v179
	v_exp_f32_e32 v180, v180
	v_exp_f32_e32 v181, v181
	v_exp_f32_e32 v182, v182
	v_exp_f32_e32 v183, v183
	v_exp_f32_e32 v184, v184
	v_exp_f32_e32 v185, v185
	v_exp_f32_e32 v186, v186
	v_exp_f32_e32 v187, v187
	v_exp_f32_e32 v188, v188
	v_exp_f32_e32 v189, v189
	v_exp_f32_e32 v190, v190
	v_exp_f32_e32 v191, v191
	v_exp_f32_e32 v192, v192
	v_exp_f32_e32 v193, v193
	v_add_f32_e32 v178, 1.0, v178
	v_add_f32_e32 v179, 1.0, v179
	v_add_f32_e32 v180, 1.0, v180
	v_add_f32_e32 v181, 1.0, v181
	v_add_f32_e32 v182, 1.0, v182
	v_add_f32_e32 v183, 1.0, v183
	v_add_f32_e32 v184, 1.0, v184
	v_add_f32_e32 v185, 1.0, v185
	v_add_f32_e32 v186, 1.0, v186
	v_add_f32_e32 v187, 1.0, v187
	v_add_f32_e32 v188, 1.0, v188
	v_add_f32_e32 v189, 1.0, v189
	v_add_f32_e32 v190, 1.0, v190
	v_add_f32_e32 v191, 1.0, v191
	v_add_f32_e32 v192, 1.0, v192
	v_add_f32_e32 v193, 1.0, v193
	v_rcp_f32_e32 v178, v178
	v_rcp_f32_e32 v179, v179
	v_rcp_f32_e32 v180, v180
	v_rcp_f32_e32 v181, v181
	v_rcp_f32_e32 v182, v182
	v_rcp_f32_e32 v183, v183
	v_rcp_f32_e32 v184, v184
	v_rcp_f32_e32 v185, v185
	v_rcp_f32_e32 v186, v186
	v_rcp_f32_e32 v187, v187
	v_rcp_f32_e32 v188, v188
	v_rcp_f32_e32 v189, v189
	v_rcp_f32_e32 v190, v190
	v_rcp_f32_e32 v191, v191
	v_rcp_f32_e32 v192, v192
	v_rcp_f32_e32 v193, v193
	v_mul_f32_e32 v178, v175, v178
	v_mul_f32_e32 v179, v175, v179
	v_mul_f32_e32 v180, v175, v180
	v_mul_f32_e32 v181, v175, v181
	v_mul_f32_e32 v182, v175, v182
	v_mul_f32_e32 v183, v175, v183
	v_mul_f32_e32 v184, v175, v184
	v_mul_f32_e32 v185, v175, v185
	v_exp_f32_e32 v104, v178
	v_exp_f32_e32 v105, v179
	v_exp_f32_e32 v106, v180
	v_exp_f32_e32 v107, v181
	v_exp_f32_e32 v108, v182
	v_exp_f32_e32 v109, v183
	v_exp_f32_e32 v110, v184
	v_exp_f32_e32 v111, v185
	s_nop 0
	v_fma_f32 v194, -v104, v104, 1.0
	v_fma_f32 v195, -v105, v105, 1.0
	v_fma_f32 v196, -v106, v106, 1.0
	v_fma_f32 v197, -v107, v107, 1.0
	v_fma_f32 v198, -v108, v108, 1.0
	v_fma_f32 v199, -v109, v109, 1.0
	v_fma_f32 v200, -v110, v110, 1.0
	v_fma_f32 v201, -v111, v111, 1.0
	v_max_f32_e32 v194, 0, v194
	v_max_f32_e32 v195, 0, v195
	v_max_f32_e32 v196, 0, v196
	v_max_f32_e32 v197, 0, v197
	v_max_f32_e32 v198, 0, v198
	v_max_f32_e32 v199, 0, v199
	v_max_f32_e32 v200, 0, v200
	v_max_f32_e32 v201, 0, v201
	v_sqrt_f32_e32 v194, v194
	v_sqrt_f32_e32 v195, v195
	v_sqrt_f32_e32 v196, v196
	v_sqrt_f32_e32 v197, v197
	v_sqrt_f32_e32 v198, v198
	v_sqrt_f32_e32 v199, v199
	v_sqrt_f32_e32 v200, v200
	v_sqrt_f32_e32 v201, v201
	s_waitcnt lgkmcnt(0)
	v_lshlrev_b32_e32 v152, 16, v152
	v_lshlrev_b32_e32 v153, 16, v153
	v_lshlrev_b32_e32 v154, 16, v154
	v_lshlrev_b32_e32 v155, 16, v155
	v_lshlrev_b32_e32 v156, 16, v156
	v_lshlrev_b32_e32 v157, 16, v157
	v_lshlrev_b32_e32 v158, 16, v158
	v_lshlrev_b32_e32 v159, 16, v159
	v_mul_f32_e32 v194, v194, v186
	v_mul_f32_e32 v195, v195, v187
	v_mul_f32_e32 v196, v196, v188
	v_mul_f32_e32 v197, v197, v189
	v_mul_f32_e32 v198, v198, v190
	v_mul_f32_e32 v199, v199, v191
	v_mul_f32_e32 v200, v200, v192
	v_mul_f32_e32 v201, v201, v193
	v_mul_f32_e32 v152, v194, v152
	v_mul_f32_e32 v153, v195, v153
	v_mul_f32_e32 v154, v196, v154
	v_mul_f32_e32 v155, v197, v155
	v_mul_f32_e32 v156, v198, v156
	v_mul_f32_e32 v157, v199, v157
	v_mul_f32_e32 v158, v200, v158
	v_mul_f32_e32 v159, v201, v159
	v_fma_f32 v145, v97, v144, v145
	v_fma_f32 v149, v101, v148, v149
	v_fma_f32 v153, v105, v152, v153
	v_fma_f32 v157, v109, v156, v157
	v_mul_f32_e32 v97, v97, v96
	v_mul_f32_e32 v101, v101, v100
	v_mul_f32_e32 v105, v105, v104
	v_mul_f32_e32 v109, v109, v108
	v_fma_f32 v146, v98, v145, v146
	v_fma_f32 v150, v102, v149, v150
	v_fma_f32 v154, v106, v153, v154
	v_fma_f32 v158, v110, v157, v158
	v_mul_f32_e32 v98, v98, v97
	v_mul_f32_e32 v102, v102, v101
	v_mul_f32_e32 v106, v106, v105
	v_mul_f32_e32 v110, v110, v109
	v_fma_f32 v147, v99, v146, v147
	v_fma_f32 v151, v103, v150, v151
	v_fma_f32 v155, v107, v154, v155
	v_fma_f32 v159, v111, v158, v159
	v_mul_f32_e32 v99, v99, v98
	v_mul_f32_e32 v103, v103, v102
	v_mul_f32_e32 v107, v107, v106
	v_mul_f32_e32 v111, v111, v110
	ds_bpermute_b32 v178, v204, v99
	ds_bpermute_b32 v182, v204, v147
	ds_bpermute_b32 v179, v204, v103
	ds_bpermute_b32 v183, v204, v151
	ds_bpermute_b32 v180, v204, v107
	ds_bpermute_b32 v184, v204, v155
	ds_bpermute_b32 v181, v204, v111
	ds_bpermute_b32 v185, v204, v159
	s_waitcnt lgkmcnt(0)
	v_fma_f32 v186, v182, v99, v147
	v_cndmask_b32_e64 v178, 1.0, v178, s[34:35]
	v_fma_f32 v187, v183, v103, v151
	v_cndmask_b32_e64 v179, 1.0, v179, s[34:35]
	v_fma_f32 v188, v184, v107, v155
	v_cndmask_b32_e64 v180, 1.0, v180, s[34:35]
	v_fma_f32 v189, v185, v111, v159
	v_cndmask_b32_e64 v181, 1.0, v181, s[34:35]
	v_cndmask_b32_e64 v223, v147, v186, s[34:35]
	v_mul_f32_e32 v219, v99, v178
	v_cndmask_b32_e64 v224, v151, v187, s[34:35]
	v_mul_f32_e32 v220, v103, v179
	v_cndmask_b32_e64 v225, v155, v188, s[34:35]
	v_mul_f32_e32 v221, v107, v180
	v_cndmask_b32_e64 v226, v159, v189, s[34:35]
	v_mul_f32_e32 v222, v111, v181
	ds_bpermute_b32 v178, v205, v219
	ds_bpermute_b32 v182, v205, v223
	ds_bpermute_b32 v179, v205, v220
	ds_bpermute_b32 v183, v205, v224
	ds_bpermute_b32 v180, v205, v221
	ds_bpermute_b32 v184, v205, v225
	ds_bpermute_b32 v181, v205, v222
	ds_bpermute_b32 v185, v205, v226
	s_waitcnt lgkmcnt(0)
	v_fma_f32 v186, v182, v219, v223
	v_cndmask_b32_e64 v178, 1.0, v178, s[36:37]
	v_fma_f32 v187, v183, v220, v224
	v_cndmask_b32_e64 v179, 1.0, v179, s[36:37]
	v_fma_f32 v188, v184, v221, v225
	v_cndmask_b32_e64 v180, 1.0, v180, s[36:37]
	v_fma_f32 v189, v185, v222, v226
	v_cndmask_b32_e64 v181, 1.0, v181, s[36:37]
	v_cndmask_b32_e64 v223, v223, v186, s[36:37]
	v_mul_f32_e32 v219, v219, v178
	v_cndmask_b32_e64 v224, v224, v187, s[36:37]
	v_mul_f32_e32 v220, v220, v179
	v_cndmask_b32_e64 v225, v225, v188, s[36:37]
	v_mul_f32_e32 v221, v221, v180
	v_cndmask_b32_e64 v226, v226, v189, s[36:37]
	v_mul_f32_e32 v222, v222, v181
	ds_bpermute_b32 v227, v204, v219
	ds_bpermute_b32 v231, v204, v223
	ds_bpermute_b32 v235, v206, v219
	ds_bpermute_b32 v239, v206, v223
	ds_bpermute_b32 v228, v204, v220
	ds_bpermute_b32 v232, v204, v224
	ds_bpermute_b32 v236, v206, v220
	ds_bpermute_b32 v244, v206, v224
	ds_bpermute_b32 v229, v204, v221
	ds_bpermute_b32 v233, v204, v225
	ds_bpermute_b32 v237, v206, v221
	ds_bpermute_b32 v245, v206, v225
	ds_bpermute_b32 v230, v204, v222
	ds_bpermute_b32 v234, v204, v226
	ds_bpermute_b32 v238, v206, v222
	ds_bpermute_b32 v246, v206, v226
	s_waitcnt lgkmcnt(0)
	v_cndmask_b32_e64 v227, 1.0, v227, s[34:35]
	v_cndmask_b32_e64 v231, 0, v231, s[34:35]
	v_cndmask_b32_e64 v228, 1.0, v228, s[34:35]
	v_cndmask_b32_e64 v232, 0, v232, s[34:35]
	v_cndmask_b32_e64 v229, 1.0, v229, s[34:35]
	v_cndmask_b32_e64 v233, 0, v233, s[34:35]
	v_cndmask_b32_e64 v230, 1.0, v230, s[34:35]
	v_cndmask_b32_e64 v234, 0, v234, s[34:35]
	v_mov_b32_e32 v190, v235
	v_mov_b32_e32 v194, v239
	v_mov_b32_e32 v198, v190
	v_mov_b32_e32 v201, v194
	v_fma_f32 v194, v194, v236, v244
	v_mul_f32_e32 v190, v190, v236
	v_mov_b32_e32 v199, v190
	v_mov_b32_e32 v177, v194
	v_fma_f32 v194, v194, v237, v245
	v_mul_f32_e32 v190, v190, v237
	v_mov_b32_e32 v200, v190
	v_mov_b32_e32 v203, v194
	v_fma_f32 v194, v194, v238, v246
	v_mul_f32_e32 v190, v190, v238
	v_mov_b32_e32 v191, v194
	ds_write_b64 v207, v[190:191] offset:1024
	s_waitcnt lgkmcnt(0)
	s_barrier
	ds_read_b64 v[178:179], v208 offset:1024
	ds_read_b64 v[180:181], v208 offset:1536
	s_waitcnt lgkmcnt(0)
	v_fma_f32 v182, v176, v178, v179
	v_cndmask_b32_e64 v183, v176, v182, s[38:39]
	v_fma_f32 v176, v182, v180, v181
	v_mov_b32_e32 v184, v183
	v_fma_f32 v185, v183, v198, v201
	v_fma_f32 v186, v183, v199, v177
	v_fma_f32 v187, v183, v200, v203
	v_fma_f32 v184, v184, v227, v231
	v_fma_f32 v185, v185, v228, v232
	v_fma_f32 v186, v186, v229, v233
	v_fma_f32 v187, v187, v230, v234
	v_fma_f32 v144, v184, v96, v144
	v_fma_f32 v148, v185, v100, v148
	v_fma_f32 v152, v186, v104, v152
	v_fma_f32 v156, v187, v108, v156
	v_fma_f32 v145, v184, v97, v145
	v_fma_f32 v149, v185, v101, v149
	v_fma_f32 v153, v186, v105, v153
	v_fma_f32 v157, v187, v109, v157
	v_fma_f32 v146, v184, v98, v146
	v_fma_f32 v150, v185, v102, v150
	v_fma_f32 v154, v186, v106, v154
	v_fma_f32 v158, v187, v110, v158
	v_fma_f32 v147, v184, v99, v147
	v_fma_f32 v151, v185, v103, v151
	v_fma_f32 v155, v186, v107, v155
	v_fma_f32 v159, v187, v111, v159
	v_cvt_pk_bf16_f32 v178, v144, v145
	v_cvt_pk_bf16_f32 v179, v146, v147
	v_cvt_pk_bf16_f32 v180, v148, v149
	v_cvt_pk_bf16_f32 v181, v150, v151
	v_cvt_pk_bf16_f32 v182, v152, v153
	v_cvt_pk_bf16_f32 v183, v154, v155
	v_cvt_pk_bf16_f32 v184, v156, v157
	v_cvt_pk_bf16_f32 v185, v158, v159
	global_store_dword v209, v178, s[44:45]
	global_store_dword v209, v179, s[44:45] offset:256
	global_store_dword v209, v180, s[44:45] offset:512
	global_store_dword v209, v181, s[44:45] offset:768
	global_store_dword v209, v182, s[44:45] offset:1024
	global_store_dword v209, v183, s[44:45] offset:1280
	global_store_dword v209, v184, s[44:45] offset:1536
	global_store_dword v209, v185, s[44:45] offset:1792
	s_add_i32 s13, s13, 1
	s_add_i32 s60, s60, -1
	s_cmp_lg_u32 s60, 0
	s_cbranch_scc1 .Lmylru_loop_0
	s_load_dwordx2 s[46:47], s[0:1], 0xc8
	s_load_dwordx2 s[48:49], s[0:1], 0xd8
	s_load_dwordx2 s[40:41], s[0:1], 0xe0
	s_lshl_b32 s50, s10, 8
	s_lshl_b32 s51, s11, 6
	s_add_i32 s50, s50, s51
	s_lshl_b32 s51, s8, 4
	s_add_i32 s50, s50, s51
	v_add_u32_e32 v179, s50, v160
	v_lshlrev_b32_e32 v179, 2, v179
	s_waitcnt lgkmcnt(0)
	global_load_dword v173, v179, s[46:47]
	global_load_dword v174, v179, s[48:49]
	global_load_dword v175, v179, s[40:41]
	v_cmp_gt_u32_e64 s[34:35], 48, v202
	v_cmp_gt_u32_e64 s[36:37], 32, v202
	v_add_u32_e32 v204, 16, v202
	v_add_u32_e32 v205, 32, v202
	v_mov_b32_e32 v206, v160
	s_cmp_eq_u32 s7, 0
	s_cselect_b64 s[38:39], -1, 0
	v_and_b32_e32 v204, 63, v204
	v_lshlrev_b32_e32 v204, 2, v204
	v_and_b32_e32 v205, 63, v205
	v_lshlrev_b32_e32 v205, 2, v205
	v_and_b32_e32 v206, 63, v206
	v_lshlrev_b32_e32 v206, 2, v206
	v_mov_b32_e32 v176, 0
	s_mov_b32 s53, 0xbfb8aa3b
	s_mov_b32 s13, 0
	s_barrier
	s_cmp_lt_u32 s13, 2
	s_sub_i32 s50, 1, s13
	s_lshl_b32 s50, s50, 7
	s_lshl_b32 s51, s9, 8
	s_add_i32 s51, s51, 0x8000
	s_add_i32 s51, s51, s50
	s_sub_i32 s50, 17, s13
	s_lshl_b32 s50, s50, 7
	s_lshl_b32 s59, s9, 11
	s_add_i32 s59, s59, s50
	s_cmp_lt_u32 s13, 2
	s_cselect_b32 s59, s51, s59
	s_lshl_b32 s52, s59, 11
	s_add_u32 s46, s16, s52
	s_addc_u32 s47, s17, 0
	s_lshl_b32 s52, s6, 13
	s_mov_b32 m0, s52
	s_add_i32 s52, s52, 0x400
	global_load_lds_dwordx4 v211, s[46:47]
	s_mov_b32 m0, s52
	s_add_i32 s52, s52, 0x400
	global_load_lds_dwordx4 v212, s[46:47]
	s_mov_b32 m0, s52
	s_add_i32 s52, s52, 0x400
	global_load_lds_dwordx4 v213, s[46:47]
	s_mov_b32 m0, s52
	s_add_i32 s52, s52, 0x400
	global_load_lds_dwordx4 v214, s[46:47]
	s_mov_b32 m0, s52
	s_add_i32 s52, s52, 0x400
	global_load_lds_dwordx4 v215, s[46:47]
	s_mov_b32 m0, s52
	s_add_i32 s52, s52, 0x400
	global_load_lds_dwordx4 v216, s[46:47]
	s_mov_b32 m0, s52
	s_add_i32 s52, s52, 0x400
	global_load_lds_dwordx4 v217, s[46:47]
	s_mov_b32 m0, s52
	s_nop 0
	global_load_lds_dwordx4 v218, s[46:47]
	s_waitcnt vmcnt(8)
	v_mul_f32_e32 v173, s53, v173
	v_mul_f32_e32 v174, s53, v174
	v_mul_f32_e32 v175, s53, v175
	v_exp_f32_e32 v175, v175
	s_nop 0
	v_add_f32_e32 v180, 1.0, v175
	v_log_f32_e32 v180, v180
	v_mov_b32_e32 v181, 0x3eaaaaab
	v_fma_f32 v181, v175, v181, -0.5
	v_fma_f32 v181, v175, v181, 1.0
	v_mul_f32_e32 v181, v175, v181
	v_mul_f32_e32 v181, 0x3fb8aa3b, v181
	v_cmp_gt_f32_e32 vcc, 0x3cf5c28f, v175
	s_nop 1
	v_cndmask_b32_e32 v175, v180, v181, vcc
	v_mul_f32_e32 v175, 0xc1000000, v175
	s_waitcnt vmcnt(0)
	s_barrier
	s_cmp_eq_u32 s13, 17
	s_cbranch_scc1 .Lmylru_nodma_5
	s_add_i32 s58, s13, 1
	s_cmp_lt_u32 s58, 2
	s_sub_i32 s50, 1, s58
	s_lshl_b32 s50, s50, 7
	s_lshl_b32 s51, s9, 8
	s_add_i32 s51, s51, 0x8000
	s_add_i32 s51, s51, s50
	s_sub_i32 s50, 17, s58
	s_lshl_b32 s50, s50, 7
	s_lshl_b32 s59, s9, 11
	s_add_i32 s59, s59, s50
	s_cmp_lt_u32 s58, 2
	s_cselect_b32 s59, s51, s59
	s_lshl_b32 s52, s59, 11
	s_add_u32 s46, s16, s52
	s_addc_u32 s47, s17, 0
	s_lshl_b32 s52, s6, 13
	s_add_i32 s52, s52, 0x10000
	s_mov_b32 m0, s52
	s_add_i32 s52, s52, 0x400
	global_load_lds_dwordx4 v211, s[46:47]
	s_mov_b32 m0, s52
	s_add_i32 s52, s52, 0x400
	global_load_lds_dwordx4 v212, s[46:47]
	s_mov_b32 m0, s52
	s_add_i32 s52, s52, 0x400
	global_load_lds_dwordx4 v213, s[46:47]
	s_mov_b32 m0, s52
	s_add_i32 s52, s52, 0x400
	global_load_lds_dwordx4 v214, s[46:47]
	s_mov_b32 m0, s52
	s_add_i32 s52, s52, 0x400
	global_load_lds_dwordx4 v215, s[46:47]
	s_mov_b32 m0, s52
	s_add_i32 s52, s52, 0x400
	global_load_lds_dwordx4 v216, s[46:47]
	s_mov_b32 m0, s52
	s_add_i32 s52, s52, 0x400
	global_load_lds_dwordx4 v217, s[46:47]
	s_mov_b32 m0, s52
	s_nop 0
	global_load_lds_dwordx4 v218, s[46:47]
